# v23 + XCD stagger of the GEMM1 unit stream (XCD g starts g x 2.4 us late) so the epilogue conversion loads of the eight XCDs do not burst together
# speedup vs baseline: 1.0235x; 1.0061x over previous
.LBB0_712:
	s_or_b64 exec, exec, s[20:21]
	s_add_u32 s0, s16, 0x4ee00000
	s_addc_u32 s1, s17, 0
	v_readfirstlane_b32 s2, v0
	s_cmp_ge_i32 s47, s33
	v_lshlrev_b32_e32 v1, 2, v0
	s_waitcnt lgkmcnt(0)
	s_barrier
	s_cbranch_scc1 .LBB0_734
	v_lshlrev_b32_e32 v2, 4, v0
	v_and_b32_e32 v3, 32, v0
	v_bitop3_b32 v2, v2, v3, 48 bitop3:0x6c
	v_bfe_u32 v3, v0, 3, 25
	v_bfe_u32 v4, v0, 2, 4
	v_and_or_b32 v163, v0, 64, v2
	v_lshrrev_b32_e32 v2, 3, v0
	v_or_b32_e32 v3, 64, v3
	s_movk_i32 s5, 0x70
	v_and_or_b32 v188, v2, 48, v4
	v_and_or_b32 v189, v3, s5, v4
	v_lshrrev_b32_e32 v4, 5, v0
	v_lshrrev_b32_e32 v7, 1, v0
	v_and_b32_e32 v4, 4, v4
	v_bfe_u32 v5, v0, 2, 2
	v_and_b32_e32 v7, 24, v7
	v_or3_b32 v4, v4, v5, v7
	v_and_or_b32 v2, v2, 32, v4
	v_lshl_or_b32 v166, v2, 11, v163
	v_mul_f32_e32 v2, 0x4f7ffffe, v6
	v_cvt_u32_f32_e32 v2, v2
	s_lshr_b32 s4, s2, 6
	s_lshr_b32 s3, s2, 8
	s_lshl_b32 s5, s4, 10
	v_readfirstlane_b32 s58, v2
	s_mul_i32 s34, s34, s58
	s_add_u32 s18, s16, 0x2600000
	s_mul_hi_u32 s22, s58, s34
	s_addc_u32 s19, s17, 0
	s_abs_i32 s21, s47
	s_add_i32 s58, s58, s22
	s_mul_hi_u32 s22, s21, s58
	s_movk_i32 s20, 0x60
	s_mul_i32 s23, s22, s53
	v_and_or_b32 v3, v3, s20, v4
	s_ashr_i32 s20, s47, 31
	s_ashr_i32 s55, s46, 31
	s_sub_i32 s21, s21, s23
	s_xor_b32 s20, s20, s55
	s_add_i32 s23, s22, 1
	s_sub_i32 s24, s21, s53
	s_cmp_ge_u32 s21, s53
	s_cselect_b32 s22, s23, s22
	s_cselect_b32 s21, s24, s21
	s_add_i32 s23, s22, 1
	s_cmp_ge_u32 s21, s53
	s_cselect_b32 s21, s23, s22
	s_xor_b32 s21, s21, s20
	s_sub_i32 s20, s21, s20
	s_mul_i32 s21, s20, s46
	s_sub_i32 s21, s47, s21
	s_ashr_i32 s22, s21, 31
	s_lshr_b32 s22, s22, 30
	s_add_i32 s22, s21, s22
	s_mov_b32 s86, s79
	s_ashr_i32 s79, s22, 2
	s_and_b32 s22, s22, -4
	s_lshl_b32 s20, s20, 2
	s_sub_i32 s21, s21, s22
	s_add_i32 s38, s21, s20
	s_add_i32 s20, s79, 0
	s_add_i32 s20, s20, 0x27d40
	v_lshl_or_b32 v164, v3, 11, v163
	v_mov_b32_e32 v2, s20
	s_add_i32 s20, 0, 0x20400
	v_lshlrev_b32_e32 v3, 1, v188
	v_lshlrev_b32_e32 v5, 1, v189
	v_add_u32_e32 v4, s20, v3
	v_add_u32_e32 v7, s20, v5
	s_add_i32 s20, 0, 0x20500
	v_add_u32_e32 v3, s20, v3
	v_add_u32_e32 v5, s20, v5
	ds_read_u8 v6, v2
	ds_read_u16 v2, v4
	ds_read_u16 v4, v7
	ds_read_u16 v3, v3
	ds_read_u16 v5, v5
	s_waitcnt lgkmcnt(4)
	v_readfirstlane_b32 s20, v6
	s_and_b32 s20, s20, 0xff
	s_ashr_i32 s39, s38, 31
	s_lshl_b32 s22, s20, 23
	s_lshl_b64 s[20:21], s[38:39], 19
	s_add_u32 s22, s0, s22
	s_addc_u32 s23, s1, 0
	s_add_u32 s40, s22, s20
	s_addc_u32 s41, s23, s21
	s_add_i32 s59, s5, 0
	s_add_i32 s60, s59, 0x10000
	s_add_i32 s61, s59, 0x12000
	s_mov_b32 m0, s60
	s_add_u32 s20, s40, 0x40000
	global_load_lds_dwordx4 v166, s[40:41]
	s_mov_b32 m0, s61
	s_addc_u32 s21, s41, 0
	s_add_i32 s62, s59, 0x14000
	global_load_lds_dwordx4 v164, s[40:41]
	s_mov_b32 m0, s62
	s_add_i32 s63, s59, 0x16000
	global_load_lds_dwordx4 v166, s[20:21]
	s_mov_b32 m0, s63
	s_waitcnt lgkmcnt(0)
	v_lshl_or_b32 v168, v2, 11, v163
	global_load_lds_dwordx4 v164, s[20:21]
	s_mov_b32 m0, s59
	s_add_i32 s64, s59, 0x2000
	v_lshl_or_b32 v170, v4, 11, v163
	global_load_lds_dwordx4 v168, s[18:19]
	s_mov_b32 m0, s64
	s_add_i32 s65, s59, 0x4000
	v_lshl_or_b32 v172, v3, 11, v163
	global_load_lds_dwordx4 v170, s[18:19]
	s_mov_b32 m0, s65
	s_add_i32 s66, s59, 0x6000
	v_lshl_or_b32 v174, v5, 11, v163
	global_load_lds_dwordx4 v172, s[18:19]
	s_mov_b32 m0, s66
	v_mov_b32_e32 v169, 0
	global_load_lds_dwordx4 v174, s[18:19]
	v_mov_b32_e32 v167, v169
	v_mov_b32_e32 v165, v169
	v_readlane_b32 s92, v254, 5
	s_nop 3
	s_and_b32 s92, s92, 7
.Lp7_stag:
	s_cmp_eq_u32 s92, 0
	s_cbranch_scc1 .Lp7_stag_done
	s_sleep 90
	s_sub_u32 s92, s92, 1
	s_branch .Lp7_stag
.Lp7_stag_done:
	s_cmp_eq_u32 s3, 1
	s_mov_b64 s[84:85], s[80:81]
	s_mov_b32 s80, 0
	v_and_b32_e32 v249, 7, v162
	v_lshrrev_b32_e32 v250, 3, v162
	v_lshlrev_b32_e32 v248, 5, v249
	v_lshl_add_u32 v248, v250, 2, v248
	v_lshlrev_b32_e32 v251, 4, v249
	v_lshl_add_u32 v249, v250, 17, v251
	v_lshl_add_u32 v250, v250, 13, v251
	v_mov_b32_e32 v252, 0x42000000
	v_mov_b32_e32 v253, 0x42000000
	v_lshl_add_u64 v[4:5], s[40:41], 0, v[166:167]
	v_lshl_add_u64 v[2:3], s[40:41], 0, v[164:165]
	s_cselect_b64 s[20:21], -1, 0
	s_cmp_lg_u32 s3, 1
	v_mov_b32_e32 v171, v169
	s_cbranch_scc1 .LBB0_715
	s_barrier
